# v30
# baseline (speedup 1.0000x reference)
.LBB0_2:
	s_or_b64 exec, exec, s[4:5]
	v_mov_b32_e32 v3, 0
	v_lshlrev_b32_e32 v130, 2, v0
	v_and_b32_e32 v131, 63, v0
	v_readfirstlane_b32 s3, v0
	v_lshlrev_b32_e32 v204, 4, v131
	v_lshlrev_b32_e32 v222, 4, v0
	v_add_u32_e32 v223, 0x2000, v222
	v_add_u32_e32 v224, 0x4000, v222
	v_add_u32_e32 v225, 0x6000, v222
	v_add_u32_e32 v226, 0x8000, v222
	v_add_u32_e32 v227, 0xa000, v222
	v_add_u32_e32 v228, 0xc000, v222
	v_add_u32_e32 v229, 0xe000, v222
	v_add_u32_e32 v230, 0x10000, v222
	v_add_u32_e32 v231, 0x12000, v222
	v_add_u32_e32 v232, 0x14000, v222
	v_add_u32_e32 v233, 0x16000, v222
	v_add_u32_e32 v234, 0x18000, v222
	v_add_u32_e32 v235, 0x1a000, v222
	v_add_u32_e32 v236, 0x1c000, v222
	v_add_u32_e32 v237, 0x1e000, v222
	s_lshr_b32 s31, s3, 6
	s_lshl_b32 s33, s2, 21
	s_waitcnt lgkmcnt(0)
	s_mov_b64 s[40:41], s[14:15]
	s_load_dword s43, s[48:49], 0x0
	s_mov_b32 s15, 0x20000
	s_brev_b32 s14, -2
	s_and_b32 s13, s13, 0xffff
	global_load_dwordx4 v[4:7], v222, s[40:41]
	global_load_dwordx4 v[8:11], v223, s[40:41]
	global_load_dwordx4 v[12:15], v224, s[40:41]
	global_load_dwordx4 v[16:19], v225, s[40:41]
	global_load_dwordx4 v[20:23], v226, s[40:41]
	global_load_dwordx4 v[24:27], v227, s[40:41]
	global_load_dwordx4 v[28:31], v228, s[40:41]
	global_load_dwordx4 v[98:101], v229, s[40:41]
	global_load_dwordx4 v[102:105], v230, s[40:41]
	global_load_dwordx4 v[106:109], v231, s[40:41]
	global_load_dwordx4 v[110:113], v232, s[40:41]
	global_load_dwordx4 v[114:117], v233, s[40:41]
	global_load_dwordx4 v[118:121], v234, s[40:41]
	global_load_dwordx4 v[122:125], v235, s[40:41]
	global_load_dwordx4 v[126:129], v236, s[40:41]
	global_load_dwordx4 v[132:135], v237, s[40:41]
	s_load_dwordx2 s[20:21], s[0:1], 0x50
	s_load_dwordx2 s[22:23], s[0:1], 0x40
	s_load_dwordx2 s[4:5], s[0:1], 0x20
	s_load_dwordx4 s[16:19], s[0:1], 0x30
	s_lshl_b32 s6, s31, 14
	s_add_i32 s6, s6, s33
	s_or_b32 s7, s6, 0x1000
	s_or_b32 s8, s6, 0x2000
	s_or_b32 s9, s6, 0x3000
	buffer_load_dwordx4 v[34:37], v204, s[12:15], s6 offen sc0 nt sc1
	buffer_load_dwordx4 v[38:41], v204, s[12:15], s7 offen sc0 nt sc1
	buffer_load_dwordx4 v[42:45], v204, s[12:15], s8 offen sc0 nt sc1
	buffer_load_dwordx4 v[46:49], v204, s[12:15], s9 offen sc0 nt sc1
	buffer_load_dwordx4 v[50:53], v204, s[12:15], s6 offen offset:1024 sc0 nt sc1
	buffer_load_dwordx4 v[54:57], v204, s[12:15], s7 offen offset:1024 sc0 nt sc1
	buffer_load_dwordx4 v[58:61], v204, s[12:15], s8 offen offset:1024 sc0 nt sc1
	buffer_load_dwordx4 v[62:65], v204, s[12:15], s9 offen offset:1024 sc0 nt sc1
	buffer_load_dwordx4 v[66:69], v204, s[12:15], s6 offen offset:2048 sc0 nt sc1
	buffer_load_dwordx4 v[70:73], v204, s[12:15], s7 offen offset:2048 sc0 nt sc1
	buffer_load_dwordx4 v[74:77], v204, s[12:15], s8 offen offset:2048 sc0 nt sc1
	buffer_load_dwordx4 v[78:81], v204, s[12:15], s9 offen offset:2048 sc0 nt sc1
	buffer_load_dwordx4 v[82:85], v204, s[12:15], s6 offen offset:3072 sc0 nt sc1
	buffer_load_dwordx4 v[86:89], v204, s[12:15], s7 offen offset:3072 sc0 nt sc1
	buffer_load_dwordx4 v[90:93], v204, s[12:15], s8 offen offset:3072 sc0 nt sc1
	buffer_load_dwordx4 v[94:97], v204, s[12:15], s9 offen offset:3072 sc0 nt sc1
	v_lshlrev_b32_e32 v2, 3, v0
	v_and_b32_e32 v1, 0x1f8, v2
	v_lshrrev_b32_e32 v32, 6, v0
	s_movk_i32 s6, 0x220
	s_waitcnt vmcnt(31)
	v_cvt_pk_bf16_f32 v4, v4, v5
	v_cvt_pk_bf16_f32 v5, v6, v7
	v_mad_u32_u24 v6, v32, s6, v1
	ds_write_b64 v6, v[4:5]
	v_add_u32_e32 v4, 0x200, v0
	v_lshrrev_b32_e32 v7, 6, v4
	s_waitcnt vmcnt(30)
	v_cvt_pk_bf16_f32 v4, v8, v9
	v_cvt_pk_bf16_f32 v5, v10, v11
	v_mad_u32_u24 v7, v7, s6, v1
	ds_write_b64 v7, v[4:5]
	s_waitcnt vmcnt(29)
	v_cvt_pk_bf16_f32 v4, v12, v13
	v_cvt_pk_bf16_f32 v5, v14, v15
	ds_write_b64 v6, v[4:5] offset:8704
	v_add_u32_e32 v4, 0x600, v0
	v_lshrrev_b32_e32 v7, 6, v4
	s_waitcnt vmcnt(28)
	v_cvt_pk_bf16_f32 v4, v16, v17
	v_cvt_pk_bf16_f32 v5, v18, v19
	v_mad_u32_u24 v7, v7, s6, v1
	ds_write_b64 v7, v[4:5]
	s_waitcnt vmcnt(27)
	v_cvt_pk_bf16_f32 v4, v20, v21
	v_cvt_pk_bf16_f32 v5, v22, v23
	ds_write_b64 v6, v[4:5] offset:17408
	v_add_u32_e32 v4, 0xa00, v0
	v_lshrrev_b32_e32 v7, 6, v4
	s_waitcnt vmcnt(26)
	v_cvt_pk_bf16_f32 v4, v24, v25
	v_cvt_pk_bf16_f32 v5, v26, v27
	v_mad_u32_u24 v7, v7, s6, v1
	ds_write_b64 v7, v[4:5]
	s_waitcnt vmcnt(25)
	v_cvt_pk_bf16_f32 v4, v28, v29
	v_cvt_pk_bf16_f32 v5, v30, v31
	ds_write_b64 v6, v[4:5] offset:26112
	v_add_u32_e32 v4, 0xe00, v0
	v_lshrrev_b32_e32 v7, 6, v4
	s_waitcnt vmcnt(24)
	v_cvt_pk_bf16_f32 v4, v98, v99
	v_cvt_pk_bf16_f32 v5, v100, v101
	v_mad_u32_u24 v7, v7, s6, v1
	ds_write_b64 v7, v[4:5]
	s_waitcnt vmcnt(23)
	v_cvt_pk_bf16_f32 v4, v102, v103
	v_cvt_pk_bf16_f32 v5, v104, v105
	ds_write_b64 v6, v[4:5] offset:34816
	v_add_u32_e32 v4, 0x1200, v0
	v_lshrrev_b32_e32 v7, 6, v4
	s_waitcnt vmcnt(22)
	v_cvt_pk_bf16_f32 v4, v106, v107
	v_cvt_pk_bf16_f32 v5, v108, v109
	v_mad_u32_u24 v7, v7, s6, v1
	ds_write_b64 v7, v[4:5]
	s_waitcnt vmcnt(21)
	v_cvt_pk_bf16_f32 v4, v110, v111
	v_cvt_pk_bf16_f32 v5, v112, v113
	ds_write_b64 v6, v[4:5] offset:43520
	v_add_u32_e32 v4, 0x1600, v0
	v_lshrrev_b32_e32 v7, 6, v4
	s_waitcnt vmcnt(20)
	v_cvt_pk_bf16_f32 v4, v114, v115
	v_cvt_pk_bf16_f32 v5, v116, v117
	v_mad_u32_u24 v7, v7, s6, v1
	ds_write_b64 v7, v[4:5]
	s_waitcnt vmcnt(19)
	v_cvt_pk_bf16_f32 v4, v118, v119
	v_cvt_pk_bf16_f32 v5, v120, v121
	ds_write_b64 v6, v[4:5] offset:52224
	v_add_u32_e32 v4, 0x1a00, v0
	v_lshrrev_b32_e32 v7, 6, v4
	s_waitcnt vmcnt(18)
	v_cvt_pk_bf16_f32 v4, v122, v123
	v_cvt_pk_bf16_f32 v5, v124, v125
	v_mad_u32_u24 v7, v7, s6, v1
	ds_write_b64 v7, v[4:5]
	s_waitcnt vmcnt(17)
	v_cvt_pk_bf16_f32 v4, v126, v127
	v_cvt_pk_bf16_f32 v5, v128, v129
	ds_write_b64 v6, v[4:5] offset:60928
	v_add_u32_e32 v4, 0x1e00, v0
	v_lshrrev_b32_e32 v6, 6, v4
	s_waitcnt vmcnt(16)
	v_cvt_pk_bf16_f32 v4, v132, v133
	v_cvt_pk_bf16_f32 v5, v134, v135
	v_mad_u32_u24 v1, v6, s6, v1
	ds_write_b64 v1, v[4:5]
	s_and_saveexec_b64 s[6:7], s[10:11]
	s_cbranch_execz .LBB0_4
	s_load_dwordx4 s[24:27], s[0:1], 0x10
	v_mov_b32_e32 v1, v3
	v_lshlrev_b64 v[4:5], 2, v[0:1]
	s_waitcnt lgkmcnt(0)
	v_lshl_add_u64 v[6:7], s[24:25], 0, v[4:5]
	global_load_dword v1, v[6:7], off
	v_lshl_add_u64 v[4:5], s[26:27], 0, v[4:5]
	global_load_dword v4, v[4:5], off
	v_add_u32_e32 v5, 0x22000, v130
	v_add_u32_e32 v6, 0x22200, v130
	s_waitcnt vmcnt(1)
	v_mul_f32_e32 v1, 0x4038aa3b, v1
	ds_write_b32 v5, v1
	s_waitcnt vmcnt(0)
	ds_write_b32 v6, v4

.LBB0_15:
	s_andn2_b64 vcc, exec, s[24:25]
	s_cbranch_vccnz .LBB0_17
	s_lshl_b32 s24, s26, 14
	s_add_i32 s24, s24, s33
	s_or_b32 s25, s24, 0x1000
	s_or_b32 s27, s24, 0x2000
	s_or_b32 s28, s24, 0x3000
	buffer_load_dwordx4 v[34:37], v204, s[12:15], s24 offen sc0 nt sc1
	buffer_load_dwordx4 v[38:41], v204, s[12:15], s25 offen sc0 nt sc1
	buffer_load_dwordx4 v[42:45], v204, s[12:15], s27 offen sc0 nt sc1
	buffer_load_dwordx4 v[46:49], v204, s[12:15], s28 offen sc0 nt sc1
	buffer_load_dwordx4 v[50:53], v204, s[12:15], s24 offen offset:1024 sc0 nt sc1
	buffer_load_dwordx4 v[54:57], v204, s[12:15], s25 offen offset:1024 sc0 nt sc1
	buffer_load_dwordx4 v[58:61], v204, s[12:15], s27 offen offset:1024 sc0 nt sc1
	buffer_load_dwordx4 v[62:65], v204, s[12:15], s28 offen offset:1024 sc0 nt sc1
	buffer_load_dwordx4 v[66:69], v204, s[12:15], s24 offen offset:2048 sc0 nt sc1
	buffer_load_dwordx4 v[70:73], v204, s[12:15], s25 offen offset:2048 sc0 nt sc1
	buffer_load_dwordx4 v[74:77], v204, s[12:15], s27 offen offset:2048 sc0 nt sc1
	buffer_load_dwordx4 v[78:81], v204, s[12:15], s28 offen offset:2048 sc0 nt sc1
	buffer_load_dwordx4 v[82:85], v204, s[12:15], s24 offen offset:3072 sc0 nt sc1
	buffer_load_dwordx4 v[86:89], v204, s[12:15], s25 offen offset:3072 sc0 nt sc1
	buffer_load_dwordx4 v[90:93], v204, s[12:15], s27 offen offset:3072 sc0 nt sc1
	buffer_load_dwordx4 v[94:97], v204, s[12:15], s28 offen offset:3072 sc0 nt sc1
